# gemm: B-operand LDS-DMAs issued half an iteration earlier (all 6 pieces of tile kt+3 in the post-barrier block, slots 0,3,6,9,12,15; tile 2 fully prefetched in the prologue)
# speedup vs baseline: 1.0149x; 1.0149x over previous
.Lgemm_T_loop:
	s_waitcnt lgkmcnt(9)
	v_mfma_f32_16x16x32_f16 v[82:85], v[134:137], v[86:89], v[82:85]
	v_mfma_f32_16x16x32_f16 v[58:61], v[138:141], v[86:89], v[58:61]
	v_mfma_f32_16x16x32_f16 v[14:17], v[142:145], v[86:89], v[14:17]
	v_mfma_f32_16x16x32_f16 v[78:81], v[134:137], v[90:93], v[78:81]
	v_mfma_f32_16x16x32_f16 v[22:25], v[138:141], v[90:93], v[22:25]
	v_mfma_f32_16x16x32_f16 v[30:33], v[142:145], v[90:93], v[30:33]
	v_mfma_f32_16x16x32_f16 v[74:77], v[134:137], v[94:97], v[74:77]
	v_mfma_f32_16x16x32_f16 v[18:21], v[138:141], v[94:97], v[18:21]
	v_mfma_f32_16x16x32_f16 v[26:29], v[142:145], v[94:97], v[26:29]
	v_mfma_f32_16x16x32_f16 v[70:73], v[134:137], v[98:101], v[70:73]
	v_mfma_f32_16x16x32_f16 v[46:49], v[138:141], v[98:101], v[46:49]
	v_mfma_f32_16x16x32_f16 v[240:243], v[142:145], v[98:101], v[240:243]
	v_mfma_f32_16x16x32_f16 v[66:69], v[134:137], v[102:105], v[66:69]
	v_mfma_f32_16x16x32_f16 v[42:45], v[138:141], v[102:105], v[42:45]
	v_mfma_f32_16x16x32_f16 v[236:239], v[142:145], v[102:105], v[236:239]
	v_mfma_f32_16x16x32_f16 v[62:65], v[134:137], v[106:109], v[62:65]
	v_mfma_f32_16x16x32_f16 v[38:41], v[138:141], v[106:109], v[38:41]
	v_mfma_f32_16x16x32_f16 v[34:37], v[142:145], v[106:109], v[34:37]
	s_waitcnt vmcnt(6) lgkmcnt(0)
	s_barrier
	s_add_u32 m0, s11, 0x0
	ds_read_b128 v[134:137], v162 offset:49152
	global_load_lds_dwordx4 v[218:219], off
	v_mfma_f32_16x16x32_f16 v[82:85], v[146:149], v[110:113], v[82:85]
	ds_read_b128 v[138:141], v162 offset:51200
	v_mfma_f32_16x16x32_f16 v[58:61], v[150:153], v[110:113], v[58:61]
	ds_read_b128 v[142:145], v162 offset:53248
	v_mfma_f32_16x16x32_f16 v[14:17], v[154:157], v[110:113], v[14:17]
	s_add_u32 m0, s11, 0x6000
	ds_read_b128 v[86:89], v158 offset:49152
	global_load_lds_dwordx4 v[220:221], off
	v_mfma_f32_16x16x32_f16 v[78:81], v[146:149], v[114:117], v[78:81]
	ds_read_b128 v[90:93], v158 offset:51200
	v_mfma_f32_16x16x32_f16 v[22:25], v[150:153], v[114:117], v[22:25]
	ds_read_b128 v[94:97], v158 offset:53248
	v_mfma_f32_16x16x32_f16 v[30:33], v[154:157], v[114:117], v[30:33]
	s_add_u32 m0, s11, 0x2000
	ds_read_b128 v[98:101], v158 offset:55296
	global_load_lds_dwordx4 v[222:223], off
	v_mfma_f32_16x16x32_f16 v[74:77], v[146:149], v[118:121], v[74:77]
	ds_read_b128 v[102:105], v158 offset:57344
	v_mfma_f32_16x16x32_f16 v[18:21], v[150:153], v[118:121], v[18:21]
	ds_read_b128 v[106:109], v158 offset:59392
	v_mfma_f32_16x16x32_f16 v[26:29], v[154:157], v[118:121], v[26:29]
	s_add_u32 m0, s11, 0x8000
	ds_read_b128 v[110:113], v160 offset:49152
	global_load_lds_dwordx4 v[224:225], off
	v_mfma_f32_16x16x32_f16 v[70:73], v[146:149], v[122:125], v[70:73]
	ds_read_b128 v[114:117], v160 offset:51200
	v_mfma_f32_16x16x32_f16 v[46:49], v[150:153], v[122:125], v[46:49]
	v_mfma_f32_16x16x32_f16 v[240:243], v[154:157], v[122:125], v[240:243]
	s_add_u32 m0, s11, 0x4000
	ds_read_b128 v[118:121], v160 offset:53248
	global_load_lds_dwordx4 v[226:227], off
	v_mfma_f32_16x16x32_f16 v[66:69], v[146:149], v[126:129], v[66:69]
	ds_read_b128 v[122:125], v160 offset:55296
	v_mfma_f32_16x16x32_f16 v[42:45], v[150:153], v[126:129], v[42:45]
	v_mfma_f32_16x16x32_f16 v[236:239], v[154:157], v[126:129], v[236:239]
	s_add_u32 m0, s11, 0xa000
	ds_read_b128 v[126:129], v160 offset:57344
	global_load_lds_dwordx4 v[228:229], off
	v_mfma_f32_16x16x32_f16 v[62:65], v[146:149], v[130:133], v[62:65]
	v_mfma_f32_16x16x32_f16 v[38:41], v[150:153], v[130:133], v[38:41]
	v_mfma_f32_16x16x32_f16 v[34:37], v[154:157], v[130:133], v[34:37]
	ds_read_b128 v[130:133], v160 offset:59392
	ds_read_b128 v[146:149], v164 offset:49152
	ds_read_b128 v[150:153], v164 offset:51200
	ds_read_b128 v[154:157], v164 offset:53248
	s_waitcnt lgkmcnt(9)
	v_mfma_f32_16x16x32_f16 v[82:85], v[134:137], v[86:89], v[82:85]
	v_mfma_f32_16x16x32_f16 v[58:61], v[138:141], v[86:89], v[58:61]
	v_mfma_f32_16x16x32_f16 v[14:17], v[142:145], v[86:89], v[14:17]
	v_mfma_f32_16x16x32_f16 v[78:81], v[134:137], v[90:93], v[78:81]
	v_mfma_f32_16x16x32_f16 v[22:25], v[138:141], v[90:93], v[22:25]
	v_mfma_f32_16x16x32_f16 v[30:33], v[142:145], v[90:93], v[30:33]
	v_mfma_f32_16x16x32_f16 v[74:77], v[134:137], v[94:97], v[74:77]
	v_mfma_f32_16x16x32_f16 v[18:21], v[138:141], v[94:97], v[18:21]
	v_mfma_f32_16x16x32_f16 v[26:29], v[142:145], v[94:97], v[26:29]
	v_mfma_f32_16x16x32_f16 v[70:73], v[134:137], v[98:101], v[70:73]
	v_mfma_f32_16x16x32_f16 v[46:49], v[138:141], v[98:101], v[46:49]
	v_mfma_f32_16x16x32_f16 v[240:243], v[142:145], v[98:101], v[240:243]
	v_mfma_f32_16x16x32_f16 v[66:69], v[134:137], v[102:105], v[66:69]
	v_mfma_f32_16x16x32_f16 v[42:45], v[138:141], v[102:105], v[42:45]
	v_mfma_f32_16x16x32_f16 v[236:239], v[142:145], v[102:105], v[236:239]
	v_mfma_f32_16x16x32_f16 v[62:65], v[134:137], v[106:109], v[62:65]
	v_mfma_f32_16x16x32_f16 v[38:41], v[138:141], v[106:109], v[38:41]
	v_mfma_f32_16x16x32_f16 v[34:37], v[142:145], v[106:109], v[34:37]
	s_waitcnt vmcnt(6) lgkmcnt(0)
	s_barrier
	s_add_u32 m0, s11, 0xbf80
	ds_read_b128 v[134:137], v163
	global_load_lds_dwordx4 v[218:219], off offset:128
	v_mfma_f32_16x16x32_f16 v[82:85], v[146:149], v[110:113], v[82:85]
	ds_read_b128 v[138:141], v163 offset:2048
	v_mfma_f32_16x16x32_f16 v[58:61], v[150:153], v[110:113], v[58:61]
	ds_read_b128 v[142:145], v163 offset:4096
	v_mfma_f32_16x16x32_f16 v[14:17], v[154:157], v[110:113], v[14:17]
	s_add_u32 m0, s11, 0x11f80
	ds_read_b128 v[86:89], v159
	global_load_lds_dwordx4 v[220:221], off offset:128
	v_mfma_f32_16x16x32_f16 v[78:81], v[146:149], v[114:117], v[78:81]
	ds_read_b128 v[90:93], v159 offset:2048
	v_mfma_f32_16x16x32_f16 v[22:25], v[150:153], v[114:117], v[22:25]
	ds_read_b128 v[94:97], v159 offset:4096
	v_mfma_f32_16x16x32_f16 v[30:33], v[154:157], v[114:117], v[30:33]
	s_add_u32 m0, s11, 0xdf80
	ds_read_b128 v[98:101], v159 offset:6144
	global_load_lds_dwordx4 v[222:223], off offset:128
	v_mfma_f32_16x16x32_f16 v[74:77], v[146:149], v[118:121], v[74:77]
	ds_read_b128 v[102:105], v159 offset:8192
	v_mfma_f32_16x16x32_f16 v[18:21], v[150:153], v[118:121], v[18:21]
	ds_read_b128 v[106:109], v159 offset:10240
	v_mfma_f32_16x16x32_f16 v[26:29], v[154:157], v[118:121], v[26:29]
	s_add_u32 m0, s11, 0x13f80
	ds_read_b128 v[110:113], v161
	global_load_lds_dwordx4 v[224:225], off offset:128
	v_mfma_f32_16x16x32_f16 v[70:73], v[146:149], v[122:125], v[70:73]
	ds_read_b128 v[114:117], v161 offset:2048
	v_mfma_f32_16x16x32_f16 v[46:49], v[150:153], v[122:125], v[46:49]
	v_mfma_f32_16x16x32_f16 v[240:243], v[154:157], v[122:125], v[240:243]
	s_add_u32 m0, s11, 0xff80
	ds_read_b128 v[118:121], v161 offset:4096
	global_load_lds_dwordx4 v[226:227], off offset:128
	v_mfma_f32_16x16x32_f16 v[66:69], v[146:149], v[126:129], v[66:69]
	ds_read_b128 v[122:125], v161 offset:6144
	v_mfma_f32_16x16x32_f16 v[42:45], v[150:153], v[126:129], v[42:45]
	v_mfma_f32_16x16x32_f16 v[236:239], v[154:157], v[126:129], v[236:239]
	s_add_u32 m0, s11, 0x15f80
	ds_read_b128 v[126:129], v161 offset:8192
	global_load_lds_dwordx4 v[228:229], off offset:128
	v_mfma_f32_16x16x32_f16 v[62:65], v[146:149], v[130:133], v[62:65]
	v_mfma_f32_16x16x32_f16 v[38:41], v[150:153], v[130:133], v[38:41]
	v_mfma_f32_16x16x32_f16 v[34:37], v[154:157], v[130:133], v[34:37]
	ds_read_b128 v[130:133], v161 offset:10240
	ds_read_b128 v[146:149], v165
	ds_read_b128 v[150:153], v165 offset:2048
	ds_read_b128 v[154:157], v165 offset:4096
	s_waitcnt lgkmcnt(9)
	v_mfma_f32_16x16x32_f16 v[82:85], v[134:137], v[86:89], v[82:85]
	v_mfma_f32_16x16x32_f16 v[58:61], v[138:141], v[86:89], v[58:61]
	v_mfma_f32_16x16x32_f16 v[14:17], v[142:145], v[86:89], v[14:17]
	v_mfma_f32_16x16x32_f16 v[78:81], v[134:137], v[90:93], v[78:81]
	v_mfma_f32_16x16x32_f16 v[22:25], v[138:141], v[90:93], v[22:25]
	v_mfma_f32_16x16x32_f16 v[30:33], v[142:145], v[90:93], v[30:33]
	v_mfma_f32_16x16x32_f16 v[74:77], v[134:137], v[94:97], v[74:77]
	v_mfma_f32_16x16x32_f16 v[18:21], v[138:141], v[94:97], v[18:21]
	v_mfma_f32_16x16x32_f16 v[26:29], v[142:145], v[94:97], v[26:29]
	v_mfma_f32_16x16x32_f16 v[70:73], v[134:137], v[98:101], v[70:73]
	v_mfma_f32_16x16x32_f16 v[46:49], v[138:141], v[98:101], v[46:49]
	v_mfma_f32_16x16x32_f16 v[240:243], v[142:145], v[98:101], v[240:243]
	v_mfma_f32_16x16x32_f16 v[66:69], v[134:137], v[102:105], v[66:69]
	v_mfma_f32_16x16x32_f16 v[42:45], v[138:141], v[102:105], v[42:45]
	v_mfma_f32_16x16x32_f16 v[236:239], v[142:145], v[102:105], v[236:239]
	v_mfma_f32_16x16x32_f16 v[62:65], v[134:137], v[106:109], v[62:65]
	v_mfma_f32_16x16x32_f16 v[38:41], v[138:141], v[106:109], v[38:41]
	v_mfma_f32_16x16x32_f16 v[34:37], v[142:145], v[106:109], v[34:37]
	s_waitcnt vmcnt(6) lgkmcnt(0)
	s_barrier
	s_add_u32 m0, s11, 0x17f00
	ds_read_b128 v[134:137], v162
	global_load_lds_dwordx4 v[218:219], off offset:256
	v_mfma_f32_16x16x32_f16 v[82:85], v[146:149], v[110:113], v[82:85]
	ds_read_b128 v[138:141], v162 offset:2048
	v_mfma_f32_16x16x32_f16 v[58:61], v[150:153], v[110:113], v[58:61]
	ds_read_b128 v[142:145], v162 offset:4096
	v_mfma_f32_16x16x32_f16 v[14:17], v[154:157], v[110:113], v[14:17]
	s_add_u32 m0, s11, 0x1df00
	ds_read_b128 v[86:89], v158
	global_load_lds_dwordx4 v[220:221], off offset:256
	v_mfma_f32_16x16x32_f16 v[78:81], v[146:149], v[114:117], v[78:81]
	ds_read_b128 v[90:93], v158 offset:2048
	v_mfma_f32_16x16x32_f16 v[22:25], v[150:153], v[114:117], v[22:25]
	ds_read_b128 v[94:97], v158 offset:4096
	v_mfma_f32_16x16x32_f16 v[30:33], v[154:157], v[114:117], v[30:33]
	s_add_u32 m0, s11, 0x19f00
	ds_read_b128 v[98:101], v158 offset:6144
	global_load_lds_dwordx4 v[222:223], off offset:256
	v_mfma_f32_16x16x32_f16 v[74:77], v[146:149], v[118:121], v[74:77]
	ds_read_b128 v[102:105], v158 offset:8192
	v_mfma_f32_16x16x32_f16 v[18:21], v[150:153], v[118:121], v[18:21]
	ds_read_b128 v[106:109], v158 offset:10240
	v_mfma_f32_16x16x32_f16 v[26:29], v[154:157], v[118:121], v[26:29]
	s_add_u32 m0, s11, 0x1ff00
	ds_read_b128 v[110:113], v160
	global_load_lds_dwordx4 v[224:225], off offset:256
	v_mfma_f32_16x16x32_f16 v[70:73], v[146:149], v[122:125], v[70:73]
	ds_read_b128 v[114:117], v160 offset:2048
	v_mfma_f32_16x16x32_f16 v[46:49], v[150:153], v[122:125], v[46:49]
	v_mfma_f32_16x16x32_f16 v[240:243], v[154:157], v[122:125], v[240:243]
	s_add_u32 m0, s11, 0x1bf00
	ds_read_b128 v[118:121], v160 offset:4096
	global_load_lds_dwordx4 v[226:227], off offset:256
	v_mfma_f32_16x16x32_f16 v[66:69], v[146:149], v[126:129], v[66:69]
	ds_read_b128 v[122:125], v160 offset:6144
	v_mfma_f32_16x16x32_f16 v[42:45], v[150:153], v[126:129], v[42:45]
	v_mfma_f32_16x16x32_f16 v[236:239], v[154:157], v[126:129], v[236:239]
	s_add_u32 m0, s11, 0x21f00
	ds_read_b128 v[126:129], v160 offset:8192
	global_load_lds_dwordx4 v[228:229], off offset:256
	v_mfma_f32_16x16x32_f16 v[62:65], v[146:149], v[130:133], v[62:65]
	v_mfma_f32_16x16x32_f16 v[38:41], v[150:153], v[130:133], v[38:41]
	v_mfma_f32_16x16x32_f16 v[34:37], v[154:157], v[130:133], v[34:37]
	ds_read_b128 v[130:133], v160 offset:10240
	ds_read_b128 v[146:149], v164
	ds_read_b128 v[150:153], v164 offset:2048
	ds_read_b128 v[154:157], v164 offset:4096
	v_lshl_add_u64 v[218:219], v[218:219], 0, s[20:21]
	v_lshl_add_u64 v[222:223], v[222:223], 0, s[20:21]
	v_lshl_add_u64 v[226:227], v[226:227], 0, s[20:21]
	v_lshl_add_u64 v[220:221], v[220:221], 0, s[20:21]
	v_lshl_add_u64 v[224:225], v[224:225], 0, s[20:21]
	v_lshl_add_u64 v[228:229], v[228:229], 0, s[20:21]
	s_sub_u32 s22, s22, 1
	s_cmp_lg_u32 s22, 0
	s_cbranch_scc1 .Lgemm_T_loop
	s_waitcnt lgkmcnt(9)
	v_mfma_f32_16x16x32_f16 v[82:85], v[134:137], v[86:89], v[82:85]
	v_mfma_f32_16x16x32_f16 v[58:61], v[138:141], v[86:89], v[58:61]
	v_mfma_f32_16x16x32_f16 v[14:17], v[142:145], v[86:89], v[14:17]
	v_mfma_f32_16x16x32_f16 v[78:81], v[134:137], v[90:93], v[78:81]
	v_mfma_f32_16x16x32_f16 v[22:25], v[138:141], v[90:93], v[22:25]
	v_mfma_f32_16x16x32_f16 v[30:33], v[142:145], v[90:93], v[30:33]
	v_mfma_f32_16x16x32_f16 v[74:77], v[134:137], v[94:97], v[74:77]
	v_mfma_f32_16x16x32_f16 v[18:21], v[138:141], v[94:97], v[18:21]
	v_mfma_f32_16x16x32_f16 v[26:29], v[142:145], v[94:97], v[26:29]
	v_mfma_f32_16x16x32_f16 v[70:73], v[134:137], v[98:101], v[70:73]
	v_mfma_f32_16x16x32_f16 v[46:49], v[138:141], v[98:101], v[46:49]
	v_mfma_f32_16x16x32_f16 v[240:243], v[142:145], v[98:101], v[240:243]
	v_mfma_f32_16x16x32_f16 v[66:69], v[134:137], v[102:105], v[66:69]
	v_mfma_f32_16x16x32_f16 v[42:45], v[138:141], v[102:105], v[42:45]
	v_mfma_f32_16x16x32_f16 v[236:239], v[142:145], v[102:105], v[236:239]
	v_mfma_f32_16x16x32_f16 v[62:65], v[134:137], v[106:109], v[62:65]
	v_mfma_f32_16x16x32_f16 v[38:41], v[138:141], v[106:109], v[38:41]
	v_mfma_f32_16x16x32_f16 v[34:37], v[142:145], v[106:109], v[34:37]
	s_waitcnt vmcnt(6) lgkmcnt(0)
	s_barrier
	s_add_u32 m0, s11, 0x0
	ds_read_b128 v[134:137], v162 offset:49152
	global_load_lds_dwordx4 v[218:219], off
	v_mfma_f32_16x16x32_f16 v[82:85], v[146:149], v[110:113], v[82:85]
	ds_read_b128 v[138:141], v162 offset:51200
	v_mfma_f32_16x16x32_f16 v[58:61], v[150:153], v[110:113], v[58:61]
	ds_read_b128 v[142:145], v162 offset:53248
	v_mfma_f32_16x16x32_f16 v[14:17], v[154:157], v[110:113], v[14:17]
	s_add_u32 m0, s11, 0x6000
	ds_read_b128 v[86:89], v158 offset:49152
	global_load_lds_dwordx4 v[220:221], off
	v_mfma_f32_16x16x32_f16 v[78:81], v[146:149], v[114:117], v[78:81]
	ds_read_b128 v[90:93], v158 offset:51200
	v_mfma_f32_16x16x32_f16 v[22:25], v[150:153], v[114:117], v[22:25]
	ds_read_b128 v[94:97], v158 offset:53248
	v_mfma_f32_16x16x32_f16 v[30:33], v[154:157], v[114:117], v[30:33]
	s_add_u32 m0, s11, 0x2000
	ds_read_b128 v[98:101], v158 offset:55296
	global_load_lds_dwordx4 v[222:223], off
	v_mfma_f32_16x16x32_f16 v[74:77], v[146:149], v[118:121], v[74:77]
	ds_read_b128 v[102:105], v158 offset:57344
	v_mfma_f32_16x16x32_f16 v[18:21], v[150:153], v[118:121], v[18:21]
	ds_read_b128 v[106:109], v158 offset:59392
	v_mfma_f32_16x16x32_f16 v[26:29], v[154:157], v[118:121], v[26:29]
	s_add_u32 m0, s11, 0x8000
	ds_read_b128 v[110:113], v160 offset:49152
	global_load_lds_dwordx4 v[224:225], off
	v_mfma_f32_16x16x32_f16 v[70:73], v[146:149], v[122:125], v[70:73]
	ds_read_b128 v[114:117], v160 offset:51200
	v_mfma_f32_16x16x32_f16 v[46:49], v[150:153], v[122:125], v[46:49]
	v_mfma_f32_16x16x32_f16 v[240:243], v[154:157], v[122:125], v[240:243]
	s_add_u32 m0, s11, 0x4000
	ds_read_b128 v[118:121], v160 offset:53248
	global_load_lds_dwordx4 v[226:227], off
	v_mfma_f32_16x16x32_f16 v[66:69], v[146:149], v[126:129], v[66:69]
	ds_read_b128 v[122:125], v160 offset:55296
	v_mfma_f32_16x16x32_f16 v[42:45], v[150:153], v[126:129], v[42:45]
	v_mfma_f32_16x16x32_f16 v[236:239], v[154:157], v[126:129], v[236:239]
	s_add_u32 m0, s11, 0xa000
	ds_read_b128 v[126:129], v160 offset:57344
	global_load_lds_dwordx4 v[228:229], off
	v_mfma_f32_16x16x32_f16 v[62:65], v[146:149], v[130:133], v[62:65]
	v_mfma_f32_16x16x32_f16 v[38:41], v[150:153], v[130:133], v[38:41]
	v_mfma_f32_16x16x32_f16 v[34:37], v[154:157], v[130:133], v[34:37]
	ds_read_b128 v[130:133], v160 offset:59392
	ds_read_b128 v[146:149], v164 offset:49152
	ds_read_b128 v[150:153], v164 offset:51200
	ds_read_b128 v[154:157], v164 offset:53248
	s_waitcnt lgkmcnt(9)
	v_mfma_f32_16x16x32_f16 v[82:85], v[134:137], v[86:89], v[82:85]
	v_mfma_f32_16x16x32_f16 v[58:61], v[138:141], v[86:89], v[58:61]
	v_mfma_f32_16x16x32_f16 v[14:17], v[142:145], v[86:89], v[14:17]
	v_mfma_f32_16x16x32_f16 v[78:81], v[134:137], v[90:93], v[78:81]
	v_mfma_f32_16x16x32_f16 v[22:25], v[138:141], v[90:93], v[22:25]
	v_mfma_f32_16x16x32_f16 v[30:33], v[142:145], v[90:93], v[30:33]
	v_mfma_f32_16x16x32_f16 v[74:77], v[134:137], v[94:97], v[74:77]
	v_mfma_f32_16x16x32_f16 v[18:21], v[138:141], v[94:97], v[18:21]
	v_mfma_f32_16x16x32_f16 v[26:29], v[142:145], v[94:97], v[26:29]
	v_mfma_f32_16x16x32_f16 v[70:73], v[134:137], v[98:101], v[70:73]
	v_mfma_f32_16x16x32_f16 v[46:49], v[138:141], v[98:101], v[46:49]
	v_mfma_f32_16x16x32_f16 v[240:243], v[142:145], v[98:101], v[240:243]
	v_mfma_f32_16x16x32_f16 v[66:69], v[134:137], v[102:105], v[66:69]
	v_mfma_f32_16x16x32_f16 v[42:45], v[138:141], v[102:105], v[42:45]
	v_mfma_f32_16x16x32_f16 v[236:239], v[142:145], v[102:105], v[236:239]
	v_mfma_f32_16x16x32_f16 v[62:65], v[134:137], v[106:109], v[62:65]
	v_mfma_f32_16x16x32_f16 v[38:41], v[138:141], v[106:109], v[38:41]
	v_mfma_f32_16x16x32_f16 v[34:37], v[142:145], v[106:109], v[34:37]
	s_waitcnt vmcnt(6) lgkmcnt(0)
	s_barrier
	s_lshl_b32 s26, s17, 2
	s_add_u32 s26, s24, s26
	s_addc_u32 s27, s25, 0
	v_lshlrev_b32_e32 v50, 4, v231
	global_load_dwordx4 v[10:13], v50, s[26:27]
	global_load_dwordx4 v[6:9], v50, s[26:27] offset:64
	global_load_dwordx4 v[2:5], v50, s[26:27] offset:128
	ds_read_b128 v[134:137], v163
	v_mfma_f32_16x16x32_f16 v[82:85], v[146:149], v[110:113], v[82:85]
	ds_read_b128 v[138:141], v163 offset:2048
	v_mfma_f32_16x16x32_f16 v[58:61], v[150:153], v[110:113], v[58:61]
	ds_read_b128 v[142:145], v163 offset:4096
	v_mfma_f32_16x16x32_f16 v[14:17], v[154:157], v[110:113], v[14:17]
	ds_read_b128 v[86:89], v159
	v_mfma_f32_16x16x32_f16 v[78:81], v[146:149], v[114:117], v[78:81]
	ds_read_b128 v[90:93], v159 offset:2048
	v_mfma_f32_16x16x32_f16 v[22:25], v[150:153], v[114:117], v[22:25]
	ds_read_b128 v[94:97], v159 offset:4096
	v_mfma_f32_16x16x32_f16 v[30:33], v[154:157], v[114:117], v[30:33]
	ds_read_b128 v[98:101], v159 offset:6144
	v_mfma_f32_16x16x32_f16 v[74:77], v[146:149], v[118:121], v[74:77]
	ds_read_b128 v[102:105], v159 offset:8192
	v_mfma_f32_16x16x32_f16 v[18:21], v[150:153], v[118:121], v[18:21]
	ds_read_b128 v[106:109], v159 offset:10240
	v_mfma_f32_16x16x32_f16 v[26:29], v[154:157], v[118:121], v[26:29]
	ds_read_b128 v[110:113], v161
	v_mfma_f32_16x16x32_f16 v[70:73], v[146:149], v[122:125], v[70:73]
	ds_read_b128 v[114:117], v161 offset:2048
	v_mfma_f32_16x16x32_f16 v[46:49], v[150:153], v[122:125], v[46:49]
	v_mfma_f32_16x16x32_f16 v[240:243], v[154:157], v[122:125], v[240:243]
	ds_read_b128 v[118:121], v161 offset:4096
	v_mfma_f32_16x16x32_f16 v[66:69], v[146:149], v[126:129], v[66:69]
	ds_read_b128 v[122:125], v161 offset:6144
	v_mfma_f32_16x16x32_f16 v[42:45], v[150:153], v[126:129], v[42:45]
	v_mfma_f32_16x16x32_f16 v[236:239], v[154:157], v[126:129], v[236:239]
	ds_read_b128 v[126:129], v161 offset:8192
	v_mfma_f32_16x16x32_f16 v[62:65], v[146:149], v[130:133], v[62:65]
	v_mfma_f32_16x16x32_f16 v[38:41], v[150:153], v[130:133], v[38:41]
	v_mfma_f32_16x16x32_f16 v[34:37], v[154:157], v[130:133], v[34:37]
	ds_read_b128 v[130:133], v161 offset:10240
	ds_read_b128 v[146:149], v165
	ds_read_b128 v[150:153], v165 offset:2048
	ds_read_b128 v[154:157], v165 offset:4096
	s_waitcnt lgkmcnt(9)
	v_mfma_f32_16x16x32_f16 v[82:85], v[134:137], v[86:89], v[82:85]
	v_mfma_f32_16x16x32_f16 v[58:61], v[138:141], v[86:89], v[58:61]
	v_mfma_f32_16x16x32_f16 v[14:17], v[142:145], v[86:89], v[14:17]
	v_mfma_f32_16x16x32_f16 v[78:81], v[134:137], v[90:93], v[78:81]
	v_mfma_f32_16x16x32_f16 v[22:25], v[138:141], v[90:93], v[22:25]
	v_mfma_f32_16x16x32_f16 v[30:33], v[142:145], v[90:93], v[30:33]
	v_mfma_f32_16x16x32_f16 v[74:77], v[134:137], v[94:97], v[74:77]
	v_mfma_f32_16x16x32_f16 v[18:21], v[138:141], v[94:97], v[18:21]
	v_mfma_f32_16x16x32_f16 v[26:29], v[142:145], v[94:97], v[26:29]
	v_mfma_f32_16x16x32_f16 v[70:73], v[134:137], v[98:101], v[70:73]
	v_mfma_f32_16x16x32_f16 v[46:49], v[138:141], v[98:101], v[46:49]
	v_mfma_f32_16x16x32_f16 v[240:243], v[142:145], v[98:101], v[240:243]
	v_mfma_f32_16x16x32_f16 v[66:69], v[134:137], v[102:105], v[66:69]
	v_mfma_f32_16x16x32_f16 v[42:45], v[138:141], v[102:105], v[42:45]
	v_mfma_f32_16x16x32_f16 v[236:239], v[142:145], v[102:105], v[236:239]
	v_mfma_f32_16x16x32_f16 v[62:65], v[134:137], v[106:109], v[62:65]
	v_mfma_f32_16x16x32_f16 v[38:41], v[138:141], v[106:109], v[38:41]
	v_mfma_f32_16x16x32_f16 v[34:37], v[142:145], v[106:109], v[34:37]
	s_waitcnt vmcnt(3) lgkmcnt(0)
	s_barrier
	ds_read_b128 v[134:137], v162
	v_mfma_f32_16x16x32_f16 v[82:85], v[146:149], v[110:113], v[82:85]
	ds_read_b128 v[138:141], v162 offset:2048
	v_mfma_f32_16x16x32_f16 v[58:61], v[150:153], v[110:113], v[58:61]
	ds_read_b128 v[142:145], v162 offset:4096
	v_mfma_f32_16x16x32_f16 v[14:17], v[154:157], v[110:113], v[14:17]
	ds_read_b128 v[86:89], v158
	v_mfma_f32_16x16x32_f16 v[78:81], v[146:149], v[114:117], v[78:81]
	ds_read_b128 v[90:93], v158 offset:2048
	v_mfma_f32_16x16x32_f16 v[22:25], v[150:153], v[114:117], v[22:25]
	ds_read_b128 v[94:97], v158 offset:4096
	v_mfma_f32_16x16x32_f16 v[30:33], v[154:157], v[114:117], v[30:33]
	ds_read_b128 v[98:101], v158 offset:6144
	v_mfma_f32_16x16x32_f16 v[74:77], v[146:149], v[118:121], v[74:77]
	ds_read_b128 v[102:105], v158 offset:8192
	v_mfma_f32_16x16x32_f16 v[18:21], v[150:153], v[118:121], v[18:21]
	ds_read_b128 v[106:109], v158 offset:10240
	v_mfma_f32_16x16x32_f16 v[26:29], v[154:157], v[118:121], v[26:29]
	ds_read_b128 v[110:113], v160
	v_mfma_f32_16x16x32_f16 v[70:73], v[146:149], v[122:125], v[70:73]
	ds_read_b128 v[114:117], v160 offset:2048
	v_mfma_f32_16x16x32_f16 v[46:49], v[150:153], v[122:125], v[46:49]
	v_mfma_f32_16x16x32_f16 v[240:243], v[154:157], v[122:125], v[240:243]
	ds_read_b128 v[118:121], v160 offset:4096
	v_mfma_f32_16x16x32_f16 v[66:69], v[146:149], v[126:129], v[66:69]
	ds_read_b128 v[122:125], v160 offset:6144
	v_mfma_f32_16x16x32_f16 v[42:45], v[150:153], v[126:129], v[42:45]
	v_mfma_f32_16x16x32_f16 v[236:239], v[154:157], v[126:129], v[236:239]
	ds_read_b128 v[126:129], v160 offset:8192
	v_mfma_f32_16x16x32_f16 v[62:65], v[146:149], v[130:133], v[62:65]
	v_mfma_f32_16x16x32_f16 v[38:41], v[150:153], v[130:133], v[38:41]
	v_mfma_f32_16x16x32_f16 v[34:37], v[154:157], v[130:133], v[34:37]
	ds_read_b128 v[130:133], v160 offset:10240
	ds_read_b128 v[146:149], v164
	ds_read_b128 v[150:153], v164 offset:2048
	ds_read_b128 v[154:157], v164 offset:4096
	s_waitcnt lgkmcnt(9)
	v_mfma_f32_16x16x32_f16 v[82:85], v[134:137], v[86:89], v[82:85]
	v_mfma_f32_16x16x32_f16 v[58:61], v[138:141], v[86:89], v[58:61]
	v_mfma_f32_16x16x32_f16 v[14:17], v[142:145], v[86:89], v[14:17]
	v_mfma_f32_16x16x32_f16 v[78:81], v[134:137], v[90:93], v[78:81]
	v_mfma_f32_16x16x32_f16 v[22:25], v[138:141], v[90:93], v[22:25]
	v_mfma_f32_16x16x32_f16 v[30:33], v[142:145], v[90:93], v[30:33]
	v_mfma_f32_16x16x32_f16 v[74:77], v[134:137], v[94:97], v[74:77]
	v_mfma_f32_16x16x32_f16 v[18:21], v[138:141], v[94:97], v[18:21]
	v_mfma_f32_16x16x32_f16 v[26:29], v[142:145], v[94:97], v[26:29]
	v_mfma_f32_16x16x32_f16 v[70:73], v[134:137], v[98:101], v[70:73]
	v_mfma_f32_16x16x32_f16 v[46:49], v[138:141], v[98:101], v[46:49]
	v_mfma_f32_16x16x32_f16 v[240:243], v[142:145], v[98:101], v[240:243]
	v_mfma_f32_16x16x32_f16 v[66:69], v[134:137], v[102:105], v[66:69]
	v_mfma_f32_16x16x32_f16 v[42:45], v[138:141], v[102:105], v[42:45]
	v_mfma_f32_16x16x32_f16 v[236:239], v[142:145], v[102:105], v[236:239]
	v_mfma_f32_16x16x32_f16 v[62:65], v[134:137], v[106:109], v[62:65]
	v_mfma_f32_16x16x32_f16 v[38:41], v[138:141], v[106:109], v[38:41]
	v_mfma_f32_16x16x32_f16 v[34:37], v[142:145], v[106:109], v[34:37]
	s_waitcnt lgkmcnt(0)
	v_mfma_f32_16x16x32_f16 v[82:85], v[146:149], v[110:113], v[82:85]
	v_mfma_f32_16x16x32_f16 v[58:61], v[150:153], v[110:113], v[58:61]
	v_mfma_f32_16x16x32_f16 v[14:17], v[154:157], v[110:113], v[14:17]
	v_mfma_f32_16x16x32_f16 v[78:81], v[146:149], v[114:117], v[78:81]
	v_mfma_f32_16x16x32_f16 v[22:25], v[150:153], v[114:117], v[22:25]
	v_mfma_f32_16x16x32_f16 v[30:33], v[154:157], v[114:117], v[30:33]
	v_mfma_f32_16x16x32_f16 v[74:77], v[146:149], v[118:121], v[74:77]
	v_mfma_f32_16x16x32_f16 v[18:21], v[150:153], v[118:121], v[18:21]
	v_mfma_f32_16x16x32_f16 v[26:29], v[154:157], v[118:121], v[26:29]
	v_mfma_f32_16x16x32_f16 v[70:73], v[146:149], v[122:125], v[70:73]
	v_mfma_f32_16x16x32_f16 v[46:49], v[150:153], v[122:125], v[46:49]
	v_mfma_f32_16x16x32_f16 v[240:243], v[154:157], v[122:125], v[240:243]
	v_mfma_f32_16x16x32_f16 v[66:69], v[146:149], v[126:129], v[66:69]
	v_mfma_f32_16x16x32_f16 v[42:45], v[150:153], v[126:129], v[42:45]
	v_mfma_f32_16x16x32_f16 v[236:239], v[154:157], v[126:129], v[236:239]
	v_mfma_f32_16x16x32_f16 v[62:65], v[146:149], v[130:133], v[62:65]
	v_mfma_f32_16x16x32_f16 v[38:41], v[150:153], v[130:133], v[38:41]
	v_mfma_f32_16x16x32_f16 v[34:37], v[154:157], v[130:133], v[34:37]
	s_branch .LBB1_76
.Lgemm_N_loop:
	s_waitcnt lgkmcnt(9)
	v_mfma_f32_16x16x32_f16 v[82:85], v[86:89], v[134:137], v[82:85]
	v_mfma_f32_16x16x32_f16 v[58:61], v[86:89], v[138:141], v[58:61]
	v_mfma_f32_16x16x32_f16 v[14:17], v[86:89], v[142:145], v[14:17]
	v_mfma_f32_16x16x32_f16 v[78:81], v[90:93], v[134:137], v[78:81]
	v_mfma_f32_16x16x32_f16 v[22:25], v[90:93], v[138:141], v[22:25]
	v_mfma_f32_16x16x32_f16 v[30:33], v[90:93], v[142:145], v[30:33]
	v_mfma_f32_16x16x32_f16 v[74:77], v[94:97], v[134:137], v[74:77]
	v_mfma_f32_16x16x32_f16 v[18:21], v[94:97], v[138:141], v[18:21]
	v_mfma_f32_16x16x32_f16 v[26:29], v[94:97], v[142:145], v[26:29]
	v_mfma_f32_16x16x32_f16 v[70:73], v[98:101], v[134:137], v[70:73]
	v_mfma_f32_16x16x32_f16 v[46:49], v[98:101], v[138:141], v[46:49]
	v_mfma_f32_16x16x32_f16 v[240:243], v[98:101], v[142:145], v[240:243]
	v_mfma_f32_16x16x32_f16 v[66:69], v[102:105], v[134:137], v[66:69]
	v_mfma_f32_16x16x32_f16 v[42:45], v[102:105], v[138:141], v[42:45]
	v_mfma_f32_16x16x32_f16 v[236:239], v[102:105], v[142:145], v[236:239]
	v_mfma_f32_16x16x32_f16 v[62:65], v[106:109], v[134:137], v[62:65]
	v_mfma_f32_16x16x32_f16 v[38:41], v[106:109], v[138:141], v[38:41]
	v_mfma_f32_16x16x32_f16 v[34:37], v[106:109], v[142:145], v[34:37]
	s_waitcnt vmcnt(6) lgkmcnt(0)
	s_barrier
	s_add_u32 m0, s11, 0x0
	ds_read_b128 v[134:137], v162 offset:49152
	global_load_lds_dwordx4 v[218:219], off
	v_mfma_f32_16x16x32_f16 v[82:85], v[110:113], v[146:149], v[82:85]
	ds_read_b128 v[138:141], v162 offset:51200
	v_mfma_f32_16x16x32_f16 v[58:61], v[110:113], v[150:153], v[58:61]
	ds_read_b128 v[142:145], v162 offset:53248
	v_mfma_f32_16x16x32_f16 v[14:17], v[110:113], v[154:157], v[14:17]
	s_add_u32 m0, s11, 0x6000
	ds_read_b128 v[86:89], v158 offset:49152
	global_load_lds_dwordx4 v[220:221], off
	v_mfma_f32_16x16x32_f16 v[78:81], v[114:117], v[146:149], v[78:81]
	ds_read_b128 v[90:93], v158 offset:51200
	v_mfma_f32_16x16x32_f16 v[22:25], v[114:117], v[150:153], v[22:25]
	ds_read_b128 v[94:97], v158 offset:53248
	v_mfma_f32_16x16x32_f16 v[30:33], v[114:117], v[154:157], v[30:33]
	s_add_u32 m0, s11, 0x2000
	ds_read_b128 v[98:101], v158 offset:55296
	global_load_lds_dwordx4 v[222:223], off
	v_mfma_f32_16x16x32_f16 v[74:77], v[118:121], v[146:149], v[74:77]
	ds_read_b128 v[102:105], v158 offset:57344
	v_mfma_f32_16x16x32_f16 v[18:21], v[118:121], v[150:153], v[18:21]
	ds_read_b128 v[106:109], v158 offset:59392
	v_mfma_f32_16x16x32_f16 v[26:29], v[118:121], v[154:157], v[26:29]
	s_add_u32 m0, s11, 0x8000
	ds_read_b128 v[110:113], v160 offset:49152
	global_load_lds_dwordx4 v[224:225], off
	v_mfma_f32_16x16x32_f16 v[70:73], v[122:125], v[146:149], v[70:73]
	ds_read_b128 v[114:117], v160 offset:51200
	v_mfma_f32_16x16x32_f16 v[46:49], v[122:125], v[150:153], v[46:49]
	v_mfma_f32_16x16x32_f16 v[240:243], v[122:125], v[154:157], v[240:243]
	s_add_u32 m0, s11, 0x4000
	ds_read_b128 v[118:121], v160 offset:53248
	global_load_lds_dwordx4 v[226:227], off
	v_mfma_f32_16x16x32_f16 v[66:69], v[126:129], v[146:149], v[66:69]
	ds_read_b128 v[122:125], v160 offset:55296
	v_mfma_f32_16x16x32_f16 v[42:45], v[126:129], v[150:153], v[42:45]
	v_mfma_f32_16x16x32_f16 v[236:239], v[126:129], v[154:157], v[236:239]
	s_add_u32 m0, s11, 0xa000
	ds_read_b128 v[126:129], v160 offset:57344
	global_load_lds_dwordx4 v[228:229], off
	v_mfma_f32_16x16x32_f16 v[62:65], v[130:133], v[146:149], v[62:65]
	v_mfma_f32_16x16x32_f16 v[38:41], v[130:133], v[150:153], v[38:41]
	v_mfma_f32_16x16x32_f16 v[34:37], v[130:133], v[154:157], v[34:37]
	ds_read_b128 v[130:133], v160 offset:59392
	ds_read_b128 v[146:149], v164 offset:49152
	ds_read_b128 v[150:153], v164 offset:51200
	ds_read_b128 v[154:157], v164 offset:53248
	s_waitcnt lgkmcnt(9)
	v_mfma_f32_16x16x32_f16 v[82:85], v[86:89], v[134:137], v[82:85]
	v_mfma_f32_16x16x32_f16 v[58:61], v[86:89], v[138:141], v[58:61]
	v_mfma_f32_16x16x32_f16 v[14:17], v[86:89], v[142:145], v[14:17]
	v_mfma_f32_16x16x32_f16 v[78:81], v[90:93], v[134:137], v[78:81]
	v_mfma_f32_16x16x32_f16 v[22:25], v[90:93], v[138:141], v[22:25]
	v_mfma_f32_16x16x32_f16 v[30:33], v[90:93], v[142:145], v[30:33]
	v_mfma_f32_16x16x32_f16 v[74:77], v[94:97], v[134:137], v[74:77]
	v_mfma_f32_16x16x32_f16 v[18:21], v[94:97], v[138:141], v[18:21]
	v_mfma_f32_16x16x32_f16 v[26:29], v[94:97], v[142:145], v[26:29]
	v_mfma_f32_16x16x32_f16 v[70:73], v[98:101], v[134:137], v[70:73]
	v_mfma_f32_16x16x32_f16 v[46:49], v[98:101], v[138:141], v[46:49]
	v_mfma_f32_16x16x32_f16 v[240:243], v[98:101], v[142:145], v[240:243]
	v_mfma_f32_16x16x32_f16 v[66:69], v[102:105], v[134:137], v[66:69]
	v_mfma_f32_16x16x32_f16 v[42:45], v[102:105], v[138:141], v[42:45]
	v_mfma_f32_16x16x32_f16 v[236:239], v[102:105], v[142:145], v[236:239]
	v_mfma_f32_16x16x32_f16 v[62:65], v[106:109], v[134:137], v[62:65]
	v_mfma_f32_16x16x32_f16 v[38:41], v[106:109], v[138:141], v[38:41]
	v_mfma_f32_16x16x32_f16 v[34:37], v[106:109], v[142:145], v[34:37]
	s_waitcnt vmcnt(6) lgkmcnt(0)
	s_barrier
	s_add_u32 m0, s11, 0xbf80
	ds_read_b128 v[134:137], v163
	global_load_lds_dwordx4 v[218:219], off offset:128
	v_mfma_f32_16x16x32_f16 v[82:85], v[110:113], v[146:149], v[82:85]
	ds_read_b128 v[138:141], v163 offset:2048
	v_mfma_f32_16x16x32_f16 v[58:61], v[110:113], v[150:153], v[58:61]
	ds_read_b128 v[142:145], v163 offset:4096
	v_mfma_f32_16x16x32_f16 v[14:17], v[110:113], v[154:157], v[14:17]
	s_add_u32 m0, s11, 0x11f80
	ds_read_b128 v[86:89], v159
	global_load_lds_dwordx4 v[220:221], off offset:128
	v_mfma_f32_16x16x32_f16 v[78:81], v[114:117], v[146:149], v[78:81]
	ds_read_b128 v[90:93], v159 offset:2048
	v_mfma_f32_16x16x32_f16 v[22:25], v[114:117], v[150:153], v[22:25]
	ds_read_b128 v[94:97], v159 offset:4096
	v_mfma_f32_16x16x32_f16 v[30:33], v[114:117], v[154:157], v[30:33]
	s_add_u32 m0, s11, 0xdf80
	ds_read_b128 v[98:101], v159 offset:6144
	global_load_lds_dwordx4 v[222:223], off offset:128
	v_mfma_f32_16x16x32_f16 v[74:77], v[118:121], v[146:149], v[74:77]
	ds_read_b128 v[102:105], v159 offset:8192
	v_mfma_f32_16x16x32_f16 v[18:21], v[118:121], v[150:153], v[18:21]
	ds_read_b128 v[106:109], v159 offset:10240
	v_mfma_f32_16x16x32_f16 v[26:29], v[118:121], v[154:157], v[26:29]
	s_add_u32 m0, s11, 0x13f80
	ds_read_b128 v[110:113], v161
	global_load_lds_dwordx4 v[224:225], off offset:128
	v_mfma_f32_16x16x32_f16 v[70:73], v[122:125], v[146:149], v[70:73]
	ds_read_b128 v[114:117], v161 offset:2048
	v_mfma_f32_16x16x32_f16 v[46:49], v[122:125], v[150:153], v[46:49]
	v_mfma_f32_16x16x32_f16 v[240:243], v[122:125], v[154:157], v[240:243]
	s_add_u32 m0, s11, 0xff80
	ds_read_b128 v[118:121], v161 offset:4096
	global_load_lds_dwordx4 v[226:227], off offset:128
	v_mfma_f32_16x16x32_f16 v[66:69], v[126:129], v[146:149], v[66:69]
	ds_read_b128 v[122:125], v161 offset:6144
	v_mfma_f32_16x16x32_f16 v[42:45], v[126:129], v[150:153], v[42:45]
	v_mfma_f32_16x16x32_f16 v[236:239], v[126:129], v[154:157], v[236:239]
	s_add_u32 m0, s11, 0x15f80
	ds_read_b128 v[126:129], v161 offset:8192
	global_load_lds_dwordx4 v[228:229], off offset:128
	v_mfma_f32_16x16x32_f16 v[62:65], v[130:133], v[146:149], v[62:65]
	v_mfma_f32_16x16x32_f16 v[38:41], v[130:133], v[150:153], v[38:41]
	v_mfma_f32_16x16x32_f16 v[34:37], v[130:133], v[154:157], v[34:37]
	ds_read_b128 v[130:133], v161 offset:10240
	ds_read_b128 v[146:149], v165
	ds_read_b128 v[150:153], v165 offset:2048
	ds_read_b128 v[154:157], v165 offset:4096
	s_waitcnt lgkmcnt(9)
	v_mfma_f32_16x16x32_f16 v[82:85], v[86:89], v[134:137], v[82:85]
	v_mfma_f32_16x16x32_f16 v[58:61], v[86:89], v[138:141], v[58:61]
	v_mfma_f32_16x16x32_f16 v[14:17], v[86:89], v[142:145], v[14:17]
	v_mfma_f32_16x16x32_f16 v[78:81], v[90:93], v[134:137], v[78:81]
	v_mfma_f32_16x16x32_f16 v[22:25], v[90:93], v[138:141], v[22:25]
	v_mfma_f32_16x16x32_f16 v[30:33], v[90:93], v[142:145], v[30:33]
	v_mfma_f32_16x16x32_f16 v[74:77], v[94:97], v[134:137], v[74:77]
	v_mfma_f32_16x16x32_f16 v[18:21], v[94:97], v[138:141], v[18:21]
	v_mfma_f32_16x16x32_f16 v[26:29], v[94:97], v[142:145], v[26:29]
	v_mfma_f32_16x16x32_f16 v[70:73], v[98:101], v[134:137], v[70:73]
	v_mfma_f32_16x16x32_f16 v[46:49], v[98:101], v[138:141], v[46:49]
	v_mfma_f32_16x16x32_f16 v[240:243], v[98:101], v[142:145], v[240:243]
	v_mfma_f32_16x16x32_f16 v[66:69], v[102:105], v[134:137], v[66:69]
	v_mfma_f32_16x16x32_f16 v[42:45], v[102:105], v[138:141], v[42:45]
	v_mfma_f32_16x16x32_f16 v[236:239], v[102:105], v[142:145], v[236:239]
	v_mfma_f32_16x16x32_f16 v[62:65], v[106:109], v[134:137], v[62:65]
	v_mfma_f32_16x16x32_f16 v[38:41], v[106:109], v[138:141], v[38:41]
	v_mfma_f32_16x16x32_f16 v[34:37], v[106:109], v[142:145], v[34:37]
	s_waitcnt vmcnt(6) lgkmcnt(0)
	s_barrier
	s_add_u32 m0, s11, 0x17f00
	ds_read_b128 v[134:137], v162
	global_load_lds_dwordx4 v[218:219], off offset:256
	v_mfma_f32_16x16x32_f16 v[82:85], v[110:113], v[146:149], v[82:85]
	ds_read_b128 v[138:141], v162 offset:2048
	v_mfma_f32_16x16x32_f16 v[58:61], v[110:113], v[150:153], v[58:61]
	ds_read_b128 v[142:145], v162 offset:4096
	v_mfma_f32_16x16x32_f16 v[14:17], v[110:113], v[154:157], v[14:17]
	s_add_u32 m0, s11, 0x1df00
	ds_read_b128 v[86:89], v158
	global_load_lds_dwordx4 v[220:221], off offset:256
	v_mfma_f32_16x16x32_f16 v[78:81], v[114:117], v[146:149], v[78:81]
	ds_read_b128 v[90:93], v158 offset:2048
	v_mfma_f32_16x16x32_f16 v[22:25], v[114:117], v[150:153], v[22:25]
	ds_read_b128 v[94:97], v158 offset:4096
	v_mfma_f32_16x16x32_f16 v[30:33], v[114:117], v[154:157], v[30:33]
	s_add_u32 m0, s11, 0x19f00
	ds_read_b128 v[98:101], v158 offset:6144
	global_load_lds_dwordx4 v[222:223], off offset:256
	v_mfma_f32_16x16x32_f16 v[74:77], v[118:121], v[146:149], v[74:77]
	ds_read_b128 v[102:105], v158 offset:8192
	v_mfma_f32_16x16x32_f16 v[18:21], v[118:121], v[150:153], v[18:21]
	ds_read_b128 v[106:109], v158 offset:10240
	v_mfma_f32_16x16x32_f16 v[26:29], v[118:121], v[154:157], v[26:29]
	s_add_u32 m0, s11, 0x1ff00
	ds_read_b128 v[110:113], v160
	global_load_lds_dwordx4 v[224:225], off offset:256
	v_mfma_f32_16x16x32_f16 v[70:73], v[122:125], v[146:149], v[70:73]
	ds_read_b128 v[114:117], v160 offset:2048
	v_mfma_f32_16x16x32_f16 v[46:49], v[122:125], v[150:153], v[46:49]
	v_mfma_f32_16x16x32_f16 v[240:243], v[122:125], v[154:157], v[240:243]
	s_add_u32 m0, s11, 0x1bf00
	ds_read_b128 v[118:121], v160 offset:4096
	global_load_lds_dwordx4 v[226:227], off offset:256
	v_mfma_f32_16x16x32_f16 v[66:69], v[126:129], v[146:149], v[66:69]
	ds_read_b128 v[122:125], v160 offset:6144
	v_mfma_f32_16x16x32_f16 v[42:45], v[126:129], v[150:153], v[42:45]
	v_mfma_f32_16x16x32_f16 v[236:239], v[126:129], v[154:157], v[236:239]
	s_add_u32 m0, s11, 0x21f00
	ds_read_b128 v[126:129], v160 offset:8192
	global_load_lds_dwordx4 v[228:229], off offset:256
	v_mfma_f32_16x16x32_f16 v[62:65], v[130:133], v[146:149], v[62:65]
	v_mfma_f32_16x16x32_f16 v[38:41], v[130:133], v[150:153], v[38:41]
	v_mfma_f32_16x16x32_f16 v[34:37], v[130:133], v[154:157], v[34:37]
	ds_read_b128 v[130:133], v160 offset:10240
	ds_read_b128 v[146:149], v164
	ds_read_b128 v[150:153], v164 offset:2048
	ds_read_b128 v[154:157], v164 offset:4096
	v_lshl_add_u64 v[218:219], v[218:219], 0, s[20:21]
	v_lshl_add_u64 v[222:223], v[222:223], 0, s[20:21]
	v_lshl_add_u64 v[226:227], v[226:227], 0, s[20:21]
	v_lshl_add_u64 v[220:221], v[220:221], 0, s[20:21]
	v_lshl_add_u64 v[224:225], v[224:225], 0, s[20:21]
	v_lshl_add_u64 v[228:229], v[228:229], 0, s[20:21]
	s_sub_u32 s22, s22, 1
	s_cmp_lg_u32 s22, 0
	s_cbranch_scc1 .Lgemm_N_loop
	s_waitcnt lgkmcnt(9)
	v_mfma_f32_16x16x32_f16 v[82:85], v[86:89], v[134:137], v[82:85]
	v_mfma_f32_16x16x32_f16 v[58:61], v[86:89], v[138:141], v[58:61]
	v_mfma_f32_16x16x32_f16 v[14:17], v[86:89], v[142:145], v[14:17]
	v_mfma_f32_16x16x32_f16 v[78:81], v[90:93], v[134:137], v[78:81]
	v_mfma_f32_16x16x32_f16 v[22:25], v[90:93], v[138:141], v[22:25]
	v_mfma_f32_16x16x32_f16 v[30:33], v[90:93], v[142:145], v[30:33]
	v_mfma_f32_16x16x32_f16 v[74:77], v[94:97], v[134:137], v[74:77]
	v_mfma_f32_16x16x32_f16 v[18:21], v[94:97], v[138:141], v[18:21]
	v_mfma_f32_16x16x32_f16 v[26:29], v[94:97], v[142:145], v[26:29]
	v_mfma_f32_16x16x32_f16 v[70:73], v[98:101], v[134:137], v[70:73]
	v_mfma_f32_16x16x32_f16 v[46:49], v[98:101], v[138:141], v[46:49]
	v_mfma_f32_16x16x32_f16 v[240:243], v[98:101], v[142:145], v[240:243]
	v_mfma_f32_16x16x32_f16 v[66:69], v[102:105], v[134:137], v[66:69]
	v_mfma_f32_16x16x32_f16 v[42:45], v[102:105], v[138:141], v[42:45]
	v_mfma_f32_16x16x32_f16 v[236:239], v[102:105], v[142:145], v[236:239]
	v_mfma_f32_16x16x32_f16 v[62:65], v[106:109], v[134:137], v[62:65]
	v_mfma_f32_16x16x32_f16 v[38:41], v[106:109], v[138:141], v[38:41]
	v_mfma_f32_16x16x32_f16 v[34:37], v[106:109], v[142:145], v[34:37]
	s_waitcnt vmcnt(6) lgkmcnt(0)
	s_barrier
	s_add_u32 m0, s11, 0x0
	ds_read_b128 v[134:137], v162 offset:49152
	global_load_lds_dwordx4 v[218:219], off
	v_mfma_f32_16x16x32_f16 v[82:85], v[110:113], v[146:149], v[82:85]
	ds_read_b128 v[138:141], v162 offset:51200
	v_mfma_f32_16x16x32_f16 v[58:61], v[110:113], v[150:153], v[58:61]
	ds_read_b128 v[142:145], v162 offset:53248
	v_mfma_f32_16x16x32_f16 v[14:17], v[110:113], v[154:157], v[14:17]
	s_add_u32 m0, s11, 0x6000
	ds_read_b128 v[86:89], v158 offset:49152
	global_load_lds_dwordx4 v[220:221], off
	v_mfma_f32_16x16x32_f16 v[78:81], v[114:117], v[146:149], v[78:81]
	ds_read_b128 v[90:93], v158 offset:51200
	v_mfma_f32_16x16x32_f16 v[22:25], v[114:117], v[150:153], v[22:25]
	ds_read_b128 v[94:97], v158 offset:53248
	v_mfma_f32_16x16x32_f16 v[30:33], v[114:117], v[154:157], v[30:33]
	s_add_u32 m0, s11, 0x2000
	ds_read_b128 v[98:101], v158 offset:55296
	global_load_lds_dwordx4 v[222:223], off
	v_mfma_f32_16x16x32_f16 v[74:77], v[118:121], v[146:149], v[74:77]
	ds_read_b128 v[102:105], v158 offset:57344
	v_mfma_f32_16x16x32_f16 v[18:21], v[118:121], v[150:153], v[18:21]
	ds_read_b128 v[106:109], v158 offset:59392
	v_mfma_f32_16x16x32_f16 v[26:29], v[118:121], v[154:157], v[26:29]
	s_add_u32 m0, s11, 0x8000
	ds_read_b128 v[110:113], v160 offset:49152
	global_load_lds_dwordx4 v[224:225], off
	v_mfma_f32_16x16x32_f16 v[70:73], v[122:125], v[146:149], v[70:73]
	ds_read_b128 v[114:117], v160 offset:51200
	v_mfma_f32_16x16x32_f16 v[46:49], v[122:125], v[150:153], v[46:49]
	v_mfma_f32_16x16x32_f16 v[240:243], v[122:125], v[154:157], v[240:243]
	s_add_u32 m0, s11, 0x4000
	ds_read_b128 v[118:121], v160 offset:53248
	global_load_lds_dwordx4 v[226:227], off
	v_mfma_f32_16x16x32_f16 v[66:69], v[126:129], v[146:149], v[66:69]
	ds_read_b128 v[122:125], v160 offset:55296
	v_mfma_f32_16x16x32_f16 v[42:45], v[126:129], v[150:153], v[42:45]
	v_mfma_f32_16x16x32_f16 v[236:239], v[126:129], v[154:157], v[236:239]
	s_add_u32 m0, s11, 0xa000
	ds_read_b128 v[126:129], v160 offset:57344
	global_load_lds_dwordx4 v[228:229], off
	v_mfma_f32_16x16x32_f16 v[62:65], v[130:133], v[146:149], v[62:65]
	v_mfma_f32_16x16x32_f16 v[38:41], v[130:133], v[150:153], v[38:41]
	v_mfma_f32_16x16x32_f16 v[34:37], v[130:133], v[154:157], v[34:37]
	ds_read_b128 v[130:133], v160 offset:59392
	ds_read_b128 v[146:149], v164 offset:49152
	ds_read_b128 v[150:153], v164 offset:51200
	ds_read_b128 v[154:157], v164 offset:53248
	s_waitcnt lgkmcnt(9)
	v_mfma_f32_16x16x32_f16 v[82:85], v[86:89], v[134:137], v[82:85]
	v_mfma_f32_16x16x32_f16 v[58:61], v[86:89], v[138:141], v[58:61]
	v_mfma_f32_16x16x32_f16 v[14:17], v[86:89], v[142:145], v[14:17]
	v_mfma_f32_16x16x32_f16 v[78:81], v[90:93], v[134:137], v[78:81]
	v_mfma_f32_16x16x32_f16 v[22:25], v[90:93], v[138:141], v[22:25]
	v_mfma_f32_16x16x32_f16 v[30:33], v[90:93], v[142:145], v[30:33]
	v_mfma_f32_16x16x32_f16 v[74:77], v[94:97], v[134:137], v[74:77]
	v_mfma_f32_16x16x32_f16 v[18:21], v[94:97], v[138:141], v[18:21]
	v_mfma_f32_16x16x32_f16 v[26:29], v[94:97], v[142:145], v[26:29]
	v_mfma_f32_16x16x32_f16 v[70:73], v[98:101], v[134:137], v[70:73]
	v_mfma_f32_16x16x32_f16 v[46:49], v[98:101], v[138:141], v[46:49]
	v_mfma_f32_16x16x32_f16 v[240:243], v[98:101], v[142:145], v[240:243]
	v_mfma_f32_16x16x32_f16 v[66:69], v[102:105], v[134:137], v[66:69]
	v_mfma_f32_16x16x32_f16 v[42:45], v[102:105], v[138:141], v[42:45]
	v_mfma_f32_16x16x32_f16 v[236:239], v[102:105], v[142:145], v[236:239]
	v_mfma_f32_16x16x32_f16 v[62:65], v[106:109], v[134:137], v[62:65]
	v_mfma_f32_16x16x32_f16 v[38:41], v[106:109], v[138:141], v[38:41]
	v_mfma_f32_16x16x32_f16 v[34:37], v[106:109], v[142:145], v[34:37]
	s_waitcnt vmcnt(6) lgkmcnt(0)
	s_barrier
	s_lshl_b32 s26, s17, 2
	s_add_u32 s26, s24, s26
	s_addc_u32 s27, s25, 0
	v_lshlrev_b32_e32 v50, 2, v1
	global_load_dword v234, v50, s[26:27]
	global_load_dword v232, v50, s[26:27] offset:64
	global_load_dword v230, v50, s[26:27] offset:128
	ds_read_b128 v[134:137], v163
	v_mfma_f32_16x16x32_f16 v[82:85], v[110:113], v[146:149], v[82:85]
	ds_read_b128 v[138:141], v163 offset:2048
	v_mfma_f32_16x16x32_f16 v[58:61], v[110:113], v[150:153], v[58:61]
	ds_read_b128 v[142:145], v163 offset:4096
	v_mfma_f32_16x16x32_f16 v[14:17], v[110:113], v[154:157], v[14:17]
	ds_read_b128 v[86:89], v159
	v_mfma_f32_16x16x32_f16 v[78:81], v[114:117], v[146:149], v[78:81]
	ds_read_b128 v[90:93], v159 offset:2048
	v_mfma_f32_16x16x32_f16 v[22:25], v[114:117], v[150:153], v[22:25]
	ds_read_b128 v[94:97], v159 offset:4096
	v_mfma_f32_16x16x32_f16 v[30:33], v[114:117], v[154:157], v[30:33]
	ds_read_b128 v[98:101], v159 offset:6144
	v_mfma_f32_16x16x32_f16 v[74:77], v[118:121], v[146:149], v[74:77]
	ds_read_b128 v[102:105], v159 offset:8192
	v_mfma_f32_16x16x32_f16 v[18:21], v[118:121], v[150:153], v[18:21]
	ds_read_b128 v[106:109], v159 offset:10240
	v_mfma_f32_16x16x32_f16 v[26:29], v[118:121], v[154:157], v[26:29]
	ds_read_b128 v[110:113], v161
	v_mfma_f32_16x16x32_f16 v[70:73], v[122:125], v[146:149], v[70:73]
	ds_read_b128 v[114:117], v161 offset:2048
	v_mfma_f32_16x16x32_f16 v[46:49], v[122:125], v[150:153], v[46:49]
	v_mfma_f32_16x16x32_f16 v[240:243], v[122:125], v[154:157], v[240:243]
	ds_read_b128 v[118:121], v161 offset:4096
	v_mfma_f32_16x16x32_f16 v[66:69], v[126:129], v[146:149], v[66:69]
	ds_read_b128 v[122:125], v161 offset:6144
	v_mfma_f32_16x16x32_f16 v[42:45], v[126:129], v[150:153], v[42:45]
	v_mfma_f32_16x16x32_f16 v[236:239], v[126:129], v[154:157], v[236:239]
	ds_read_b128 v[126:129], v161 offset:8192
	v_mfma_f32_16x16x32_f16 v[62:65], v[130:133], v[146:149], v[62:65]
	v_mfma_f32_16x16x32_f16 v[38:41], v[130:133], v[150:153], v[38:41]
	v_mfma_f32_16x16x32_f16 v[34:37], v[130:133], v[154:157], v[34:37]
	ds_read_b128 v[130:133], v161 offset:10240
	ds_read_b128 v[146:149], v165
	ds_read_b128 v[150:153], v165 offset:2048
	ds_read_b128 v[154:157], v165 offset:4096
	s_waitcnt lgkmcnt(9)
	v_mfma_f32_16x16x32_f16 v[82:85], v[86:89], v[134:137], v[82:85]
	v_mfma_f32_16x16x32_f16 v[58:61], v[86:89], v[138:141], v[58:61]
	v_mfma_f32_16x16x32_f16 v[14:17], v[86:89], v[142:145], v[14:17]
	v_mfma_f32_16x16x32_f16 v[78:81], v[90:93], v[134:137], v[78:81]
	v_mfma_f32_16x16x32_f16 v[22:25], v[90:93], v[138:141], v[22:25]
	v_mfma_f32_16x16x32_f16 v[30:33], v[90:93], v[142:145], v[30:33]
	v_mfma_f32_16x16x32_f16 v[74:77], v[94:97], v[134:137], v[74:77]
	v_mfma_f32_16x16x32_f16 v[18:21], v[94:97], v[138:141], v[18:21]
	v_mfma_f32_16x16x32_f16 v[26:29], v[94:97], v[142:145], v[26:29]
	v_mfma_f32_16x16x32_f16 v[70:73], v[98:101], v[134:137], v[70:73]
	v_mfma_f32_16x16x32_f16 v[46:49], v[98:101], v[138:141], v[46:49]
	v_mfma_f32_16x16x32_f16 v[240:243], v[98:101], v[142:145], v[240:243]
	v_mfma_f32_16x16x32_f16 v[66:69], v[102:105], v[134:137], v[66:69]
	v_mfma_f32_16x16x32_f16 v[42:45], v[102:105], v[138:141], v[42:45]
	v_mfma_f32_16x16x32_f16 v[236:239], v[102:105], v[142:145], v[236:239]
	v_mfma_f32_16x16x32_f16 v[62:65], v[106:109], v[134:137], v[62:65]
	v_mfma_f32_16x16x32_f16 v[38:41], v[106:109], v[138:141], v[38:41]
	v_mfma_f32_16x16x32_f16 v[34:37], v[106:109], v[142:145], v[34:37]
	s_waitcnt vmcnt(3) lgkmcnt(0)
	s_barrier
	ds_read_b128 v[134:137], v162
	v_mfma_f32_16x16x32_f16 v[82:85], v[110:113], v[146:149], v[82:85]
	ds_read_b128 v[138:141], v162 offset:2048
	v_mfma_f32_16x16x32_f16 v[58:61], v[110:113], v[150:153], v[58:61]
	ds_read_b128 v[142:145], v162 offset:4096
	v_mfma_f32_16x16x32_f16 v[14:17], v[110:113], v[154:157], v[14:17]
	ds_read_b128 v[86:89], v158
	v_mfma_f32_16x16x32_f16 v[78:81], v[114:117], v[146:149], v[78:81]
	ds_read_b128 v[90:93], v158 offset:2048
	v_mfma_f32_16x16x32_f16 v[22:25], v[114:117], v[150:153], v[22:25]
	ds_read_b128 v[94:97], v158 offset:4096
	v_mfma_f32_16x16x32_f16 v[30:33], v[114:117], v[154:157], v[30:33]
	ds_read_b128 v[98:101], v158 offset:6144
	v_mfma_f32_16x16x32_f16 v[74:77], v[118:121], v[146:149], v[74:77]
	ds_read_b128 v[102:105], v158 offset:8192
	v_mfma_f32_16x16x32_f16 v[18:21], v[118:121], v[150:153], v[18:21]
	ds_read_b128 v[106:109], v158 offset:10240
	v_mfma_f32_16x16x32_f16 v[26:29], v[118:121], v[154:157], v[26:29]
	ds_read_b128 v[110:113], v160
	v_mfma_f32_16x16x32_f16 v[70:73], v[122:125], v[146:149], v[70:73]
	ds_read_b128 v[114:117], v160 offset:2048
	v_mfma_f32_16x16x32_f16 v[46:49], v[122:125], v[150:153], v[46:49]
	v_mfma_f32_16x16x32_f16 v[240:243], v[122:125], v[154:157], v[240:243]
	ds_read_b128 v[118:121], v160 offset:4096
	v_mfma_f32_16x16x32_f16 v[66:69], v[126:129], v[146:149], v[66:69]
	ds_read_b128 v[122:125], v160 offset:6144
	v_mfma_f32_16x16x32_f16 v[42:45], v[126:129], v[150:153], v[42:45]
	v_mfma_f32_16x16x32_f16 v[236:239], v[126:129], v[154:157], v[236:239]
	ds_read_b128 v[126:129], v160 offset:8192
	v_mfma_f32_16x16x32_f16 v[62:65], v[130:133], v[146:149], v[62:65]
	v_mfma_f32_16x16x32_f16 v[38:41], v[130:133], v[150:153], v[38:41]
	v_mfma_f32_16x16x32_f16 v[34:37], v[130:133], v[154:157], v[34:37]
	ds_read_b128 v[130:133], v160 offset:10240
	ds_read_b128 v[146:149], v164
	ds_read_b128 v[150:153], v164 offset:2048
	ds_read_b128 v[154:157], v164 offset:4096
	s_waitcnt lgkmcnt(9)
	v_mfma_f32_16x16x32_f16 v[82:85], v[86:89], v[134:137], v[82:85]
	v_mfma_f32_16x16x32_f16 v[58:61], v[86:89], v[138:141], v[58:61]
	v_mfma_f32_16x16x32_f16 v[14:17], v[86:89], v[142:145], v[14:17]
	v_mfma_f32_16x16x32_f16 v[78:81], v[90:93], v[134:137], v[78:81]
	v_mfma_f32_16x16x32_f16 v[22:25], v[90:93], v[138:141], v[22:25]
	v_mfma_f32_16x16x32_f16 v[30:33], v[90:93], v[142:145], v[30:33]
	v_mfma_f32_16x16x32_f16 v[74:77], v[94:97], v[134:137], v[74:77]
	v_mfma_f32_16x16x32_f16 v[18:21], v[94:97], v[138:141], v[18:21]
	v_mfma_f32_16x16x32_f16 v[26:29], v[94:97], v[142:145], v[26:29]
	v_mfma_f32_16x16x32_f16 v[70:73], v[98:101], v[134:137], v[70:73]
	v_mfma_f32_16x16x32_f16 v[46:49], v[98:101], v[138:141], v[46:49]
	v_mfma_f32_16x16x32_f16 v[240:243], v[98:101], v[142:145], v[240:243]
	v_mfma_f32_16x16x32_f16 v[66:69], v[102:105], v[134:137], v[66:69]
	v_mfma_f32_16x16x32_f16 v[42:45], v[102:105], v[138:141], v[42:45]
	v_mfma_f32_16x16x32_f16 v[236:239], v[102:105], v[142:145], v[236:239]
	v_mfma_f32_16x16x32_f16 v[62:65], v[106:109], v[134:137], v[62:65]
	v_mfma_f32_16x16x32_f16 v[38:41], v[106:109], v[138:141], v[38:41]
	v_mfma_f32_16x16x32_f16 v[34:37], v[106:109], v[142:145], v[34:37]
	s_waitcnt lgkmcnt(0)
	v_mfma_f32_16x16x32_f16 v[82:85], v[110:113], v[146:149], v[82:85]
	v_mfma_f32_16x16x32_f16 v[58:61], v[110:113], v[150:153], v[58:61]
	v_mfma_f32_16x16x32_f16 v[14:17], v[110:113], v[154:157], v[14:17]
	v_mfma_f32_16x16x32_f16 v[78:81], v[114:117], v[146:149], v[78:81]
	v_mfma_f32_16x16x32_f16 v[22:25], v[114:117], v[150:153], v[22:25]
	v_mfma_f32_16x16x32_f16 v[30:33], v[114:117], v[154:157], v[30:33]
	v_mfma_f32_16x16x32_f16 v[74:77], v[118:121], v[146:149], v[74:77]
	v_mfma_f32_16x16x32_f16 v[18:21], v[118:121], v[150:153], v[18:21]
	v_mfma_f32_16x16x32_f16 v[26:29], v[118:121], v[154:157], v[26:29]
	v_mfma_f32_16x16x32_f16 v[70:73], v[122:125], v[146:149], v[70:73]
	v_mfma_f32_16x16x32_f16 v[46:49], v[122:125], v[150:153], v[46:49]
	v_mfma_f32_16x16x32_f16 v[240:243], v[122:125], v[154:157], v[240:243]
	v_mfma_f32_16x16x32_f16 v[66:69], v[126:129], v[146:149], v[66:69]
	v_mfma_f32_16x16x32_f16 v[42:45], v[126:129], v[150:153], v[42:45]
	v_mfma_f32_16x16x32_f16 v[236:239], v[126:129], v[154:157], v[236:239]
	v_mfma_f32_16x16x32_f16 v[62:65], v[130:133], v[146:149], v[62:65]
	v_mfma_f32_16x16x32_f16 v[38:41], v[130:133], v[150:153], v[38:41]
	v_mfma_f32_16x16x32_f16 v[34:37], v[130:133], v[154:157], v[34:37]
